# grid barrier: acquire invalidate issued at entry, XGEN bump before leader acquire
# speedup vs baseline: 1.0111x; 1.0111x over previous
; __device__ __forceinline__ unsigned xb_ld(unsigned* p)              { return __hip_atomic_load(p, __ATOMIC_RELAXED, __HIP_MEMORY_SCOPE_AGENT); }
; __device__ __forceinline__ unsigned xb_add(unsigned* p, unsigned v) { return __hip_atomic_fetch_add(p, v, __ATOMIC_RELAXED, __HIP_MEMORY_SCOPE_AGENT); }
; #define XB_SPIN(cond, bar) do { unsigned _sp = 0; while (cond) { __builtin_amdgcn_s_sleep(1); \
;     if ((++_sp & 255u) == 0u) { if (xb_ld(&(bar)[XB_TMO])) break; if (_sp > XB_SPIN_CAP) { atomicAdd(&(bar)[XB_TMO], 1u); break; } } } } while (0)
; __device__ __forceinline__ void xcd_barrier(const XcdBarrier& b) {
;     ...
;         __builtin_amdgcn_s_waitcnt(0);
;         unsigned nloc = b.st[0], nx = b.st[1];
;         if (nloc == 0u) { xcd_barrier_complete(bar, b.x, nloc, nx); b.st[0] = nloc; b.st[1] = nx; }
;         const unsigned old = xb_add(&bar[XB_XSUB(b.x)], 1u);
;         const unsigned gen = old / nloc;
;         if (old + 1u == (gen + 1u) * nloc) {
;             __builtin_amdgcn_fence(__ATOMIC_RELEASE, "agent");
;             asm volatile("s_waitcnt vmcnt(0)" ::: "memory");
;             const unsigned og = xb_add(&bar[XB_TOP], 1u);
;             const unsigned tg = og / nx;
;             if (og + 1u == (tg + 1u) * nx) xb_add(&bar[XB_TOPGEN], 1u);
;             else XB_SPIN(xb_ld(&bar[XB_TOPGEN]) == tg, bar);
;             __builtin_amdgcn_fence(__ATOMIC_ACQUIRE, "agent");
;             xb_add(&bar[XB_XGEN(b.x)], 1u);
;             asm volatile("s_waitcnt vmcnt(0)" ::: "memory");
;         } else {
;             XB_SPIN(xb_ld(&bar[XB_XGEN(b.x)]) == gen, bar);
.LBB0_85:
	s_lshl_b32 s2, s50, 8
	s_add_u32 s6, s8, s2
	s_addc_u32 s7, s9, 0
	v_mov_b32_e32 v2, 0x1000
	v_mov_b32_e32 v4, 1
	buffer_inv sc1
	global_atomic_add v4, v2, v4, s[6:7] offset:1024 sc0
	v_cvt_f32_u32_e32 v2, v3
	v_sub_u32_e32 v5, 0, v3
	v_rcp_iflag_f32_e32 v2, v2
	s_nop 0
	v_mul_f32_e32 v2, 0x4f7ffffe, v2
	v_cvt_u32_f32_e32 v2, v2
	v_mul_lo_u32 v5, v5, v2
	v_mul_hi_u32 v5, v2, v5
	v_add_u32_e32 v2, v2, v5
	s_waitcnt vmcnt(0)
	v_mul_hi_u32 v2, v4, v2
	v_mul_lo_u32 v5, v2, v3
	v_sub_u32_e32 v5, v4, v5
	v_add_u32_e32 v6, 1, v2
	v_cmp_ge_u32_e32 vcc, v5, v3
	v_add_u32_e32 v4, 1, v4
	s_nop 0
	v_cndmask_b32_e32 v2, v2, v6, vcc
	v_sub_u32_e32 v6, v5, v3
	v_cndmask_b32_e32 v5, v5, v6, vcc
	v_add_u32_e32 v6, 1, v2
	v_cmp_ge_u32_e32 vcc, v5, v3
	s_nop 1
	v_cndmask_b32_e32 v2, v2, v6, vcc
	v_mul_lo_u32 v5, v3, v2
	v_add_u32_e32 v3, v5, v3
	v_cmp_ne_u32_e32 vcc, v4, v3
	s_and_saveexec_b64 s[10:11], vcc
	s_xor_b64 s[10:11], exec, s[10:11]
	s_cbranch_execz .LBB0_99
	s_waitcnt lgkmcnt(0)
	v_mov_b32_e32 v1, 0x2000
	global_load_dword v1, v1, s[6:7] offset:1024 sc1
	s_add_u32 s16, s6, 0x2400
	s_addc_u32 s17, s7, 0
	s_waitcnt vmcnt(0)
	v_cmp_eq_u32_e32 vcc, v1, v2
	s_and_saveexec_b64 s[12:13], vcc
	s_cbranch_execz .LBB0_98
	s_add_u32 s14, s30, 0x4200
	s_addc_u32 s15, s31, 0
	s_mov_b32 s3, 1
	s_mov_b64 s[18:19], 0
	v_mov_b32_e32 v1, 0
	s_branch .LBB0_89

; __device__ __forceinline__ unsigned xb_ld(unsigned* p)              { return __hip_atomic_load(p, __ATOMIC_RELAXED, __HIP_MEMORY_SCOPE_AGENT); }
; #define XB_SPIN(cond, bar) do { unsigned _sp = 0; while (cond) { __builtin_amdgcn_s_sleep(1); \
;     if ((++_sp & 255u) == 0u) { if (xb_ld(&(bar)[XB_TMO])) break; if (_sp > XB_SPIN_CAP) { atomicAdd(&(bar)[XB_TMO], 1u); break; } } } } while (0)
; __device__ __forceinline__ void xcd_barrier(const XcdBarrier& b) {
;     ...
;             XB_SPIN(xb_ld(&bar[XB_XGEN(b.x)]) == gen, bar);
;             __builtin_amdgcn_fence(__ATOMIC_ACQUIRE, "agent");
;             asm volatile("s_waitcnt vmcnt(0)" ::: "memory");
.LBB0_98:
	s_or_b64 exec, exec, s[12:13]
	s_waitcnt vmcnt(0)
	s_waitcnt vmcnt(0)

; __device__ __forceinline__ unsigned xb_ld(unsigned* p)              { return __hip_atomic_load(p, __ATOMIC_RELAXED, __HIP_MEMORY_SCOPE_AGENT); }
; __device__ __forceinline__ unsigned xb_add(unsigned* p, unsigned v) { return __hip_atomic_fetch_add(p, v, __ATOMIC_RELAXED, __HIP_MEMORY_SCOPE_AGENT); }
; #define XB_SPIN(cond, bar) do { unsigned _sp = 0; while (cond) { __builtin_amdgcn_s_sleep(1); \
;     if ((++_sp & 255u) == 0u) { if (xb_ld(&(bar)[XB_TMO])) break; if (_sp > XB_SPIN_CAP) { atomicAdd(&(bar)[XB_TMO], 1u); break; } } } } while (0)
; __device__ __forceinline__ void xcd_barrier(const XcdBarrier& b) {
;     ...
;             const unsigned og = xb_add(&bar[XB_TOP], 1u);
;             const unsigned tg = og / nx;
;             if (og + 1u == (tg + 1u) * nx) xb_add(&bar[XB_TOPGEN], 1u);
;             else XB_SPIN(xb_ld(&bar[XB_TOPGEN]) == tg, bar);
;             __builtin_amdgcn_fence(__ATOMIC_ACQUIRE, "agent");
;             xb_add(&bar[XB_XGEN(b.x)], 1u);
;             asm volatile("s_waitcnt vmcnt(0)" ::: "memory");
.LBB0_116:
	s_or_b64 exec, exec, s[10:11]
	v_mov_b32_e32 v1, 0x2000
	v_mov_b32_e32 v2, 1
	s_waitcnt vmcnt(0)
	global_atomic_add v1, v2, s[6:7] offset:1024
	s_waitcnt vmcnt(0)

; __device__ __forceinline__ unsigned xb_ld(unsigned* p)              { return __hip_atomic_load(p, __ATOMIC_RELAXED, __HIP_MEMORY_SCOPE_AGENT); }
; __device__ __forceinline__ unsigned xb_add(unsigned* p, unsigned v) { return __hip_atomic_fetch_add(p, v, __ATOMIC_RELAXED, __HIP_MEMORY_SCOPE_AGENT); }
; #define XB_SPIN(cond, bar) do { unsigned _sp = 0; while (cond) { __builtin_amdgcn_s_sleep(1); \
;     if ((++_sp & 255u) == 0u) { if (xb_ld(&(bar)[XB_TMO])) break; if (_sp > XB_SPIN_CAP) { atomicAdd(&(bar)[XB_TMO], 1u); break; } } } } while (0)
; __device__ __forceinline__ void xcd_barrier(const XcdBarrier& b) {
;     ...
;             const unsigned og = xb_add(&bar[XB_TOP], 1u);
;             const unsigned tg = og / nx;
;             if (og + 1u == (tg + 1u) * nx) xb_add(&bar[XB_TOPGEN], 1u);
;             else XB_SPIN(xb_ld(&bar[XB_TOPGEN]) == tg, bar);
;             __builtin_amdgcn_fence(__ATOMIC_ACQUIRE, "agent");
;             xb_add(&bar[XB_XGEN(b.x)], 1u);
;             asm volatile("s_waitcnt vmcnt(0)" ::: "memory");
.LBB0_119:
	s_or_b64 exec, exec, s[4:5]
	v_readlane_b32 s4, v251, 32
	v_readlane_b32 s5, v251, 33
	s_waitcnt vmcnt(0)
	s_nop 3
	global_atomic_add v187, v224, s[4:5]
	s_waitcnt vmcnt(0)

; __device__ __forceinline__ unsigned xb_ld(unsigned* p)              { return __hip_atomic_load(p, __ATOMIC_RELAXED, __HIP_MEMORY_SCOPE_AGENT); }
; __device__ __forceinline__ unsigned xb_add(unsigned* p, unsigned v) { return __hip_atomic_fetch_add(p, v, __ATOMIC_RELAXED, __HIP_MEMORY_SCOPE_AGENT); }
; #define XB_SPIN(cond, bar) do { unsigned _sp = 0; while (cond) { __builtin_amdgcn_s_sleep(1); \
;     if ((++_sp & 255u) == 0u) { if (xb_ld(&(bar)[XB_TMO])) break; if (_sp > XB_SPIN_CAP) { atomicAdd(&(bar)[XB_TMO], 1u); break; } } } } while (0)
; __device__ __forceinline__ void xcd_barrier(const XcdBarrier& b) {
;     ...
;         __builtin_amdgcn_s_waitcnt(0);
;         unsigned nloc = b.st[0], nx = b.st[1];
;         if (nloc == 0u) { xcd_barrier_complete(bar, b.x, nloc, nx); b.st[0] = nloc; b.st[1] = nx; }
;         const unsigned old = xb_add(&bar[XB_XSUB(b.x)], 1u);
;         const unsigned gen = old / nloc;
;         if (old + 1u == (gen + 1u) * nloc) {
;             __builtin_amdgcn_fence(__ATOMIC_RELEASE, "agent");
;             asm volatile("s_waitcnt vmcnt(0)" ::: "memory");
;             const unsigned og = xb_add(&bar[XB_TOP], 1u);
;             const unsigned tg = og / nx;
;             if (og + 1u == (tg + 1u) * nx) xb_add(&bar[XB_TOPGEN], 1u);
;             else XB_SPIN(xb_ld(&bar[XB_TOPGEN]) == tg, bar);
;             __builtin_amdgcn_fence(__ATOMIC_ACQUIRE, "agent");
;             xb_add(&bar[XB_XGEN(b.x)], 1u);
;             asm volatile("s_waitcnt vmcnt(0)" ::: "memory");
;         } else {
;             XB_SPIN(xb_ld(&bar[XB_XGEN(b.x)]) == gen, bar);
.LBB0_220:
	v_readlane_b32 s4, v251, 30
	v_readlane_b32 s5, v251, 31
	v_cvt_f32_u32_e32 v1, v3
	v_sub_u32_e32 v5, 0, v3
	v_rcp_iflag_f32_e32 v1, v1
	s_nop 1
	buffer_inv sc1
	global_atomic_add v4, v187, v224, s[4:5] sc0
	v_mul_f32_e32 v1, 0x4f7ffffe, v1
	v_cvt_u32_f32_e32 v1, v1
	v_mul_lo_u32 v5, v5, v1
	v_mul_hi_u32 v5, v1, v5
	v_add_u32_e32 v1, v1, v5
	s_waitcnt vmcnt(0)
	v_mul_hi_u32 v1, v4, v1
	v_mul_lo_u32 v5, v1, v3
	v_sub_u32_e32 v5, v4, v5
	v_add_u32_e32 v6, 1, v1
	v_cmp_ge_u32_e32 vcc, v5, v3
	v_add_u32_e32 v4, 1, v4
	s_nop 0
	v_cndmask_b32_e32 v1, v1, v6, vcc
	v_sub_u32_e32 v6, v5, v3
	v_cndmask_b32_e32 v5, v5, v6, vcc
	v_add_u32_e32 v6, 1, v1
	v_cmp_ge_u32_e32 vcc, v5, v3
	s_nop 1
	v_cndmask_b32_e32 v1, v1, v6, vcc
	v_mul_lo_u32 v5, v3, v1
	v_add_u32_e32 v3, v5, v3
	v_cmp_ne_u32_e32 vcc, v4, v3
	s_and_saveexec_b64 s[4:5], vcc
	s_xor_b64 s[4:5], exec, s[4:5]
	s_cbranch_execz .LBB0_234
	v_readlane_b32 s6, v251, 32
	v_readlane_b32 s7, v251, 33
	s_waitcnt lgkmcnt(0)
	s_nop 3
	global_load_dword v2, v187, s[6:7] sc1
	s_waitcnt vmcnt(0)
	v_cmp_eq_u32_e32 vcc, v2, v1
	s_and_saveexec_b64 s[6:7], vcc
	s_cbranch_execz .LBB0_233
	s_mov_b32 s21, 1
	s_mov_b64 s[8:9], 0
	s_branch .LBB0_224

; __device__ __forceinline__ unsigned xb_ld(unsigned* p)              { return __hip_atomic_load(p, __ATOMIC_RELAXED, __HIP_MEMORY_SCOPE_AGENT); }
; #define XB_SPIN(cond, bar) do { unsigned _sp = 0; while (cond) { __builtin_amdgcn_s_sleep(1); \
;     if ((++_sp & 255u) == 0u) { if (xb_ld(&(bar)[XB_TMO])) break; if (_sp > XB_SPIN_CAP) { atomicAdd(&(bar)[XB_TMO], 1u); break; } } } } while (0)
; __device__ __forceinline__ void xcd_barrier(const XcdBarrier& b) {
;     ...
;             XB_SPIN(xb_ld(&bar[XB_XGEN(b.x)]) == gen, bar);
;             __builtin_amdgcn_fence(__ATOMIC_ACQUIRE, "agent");
;             asm volatile("s_waitcnt vmcnt(0)" ::: "memory");
.LBB0_233:
	s_or_b64 exec, exec, s[6:7]
	s_waitcnt vmcnt(0)
	s_waitcnt vmcnt(0)

; __device__ __forceinline__ unsigned xb_ld(unsigned* p)              { return __hip_atomic_load(p, __ATOMIC_RELAXED, __HIP_MEMORY_SCOPE_AGENT); }
; __device__ __forceinline__ unsigned xb_add(unsigned* p, unsigned v) { return __hip_atomic_fetch_add(p, v, __ATOMIC_RELAXED, __HIP_MEMORY_SCOPE_AGENT); }
; #define XB_SPIN(cond, bar) do { unsigned _sp = 0; while (cond) { __builtin_amdgcn_s_sleep(1); \
;     if ((++_sp & 255u) == 0u) { if (xb_ld(&(bar)[XB_TMO])) break; if (_sp > XB_SPIN_CAP) { atomicAdd(&(bar)[XB_TMO], 1u); break; } } } } while (0)
; __device__ __forceinline__ void xcd_barrier(const XcdBarrier& b) {
;     ...
;         __builtin_amdgcn_s_waitcnt(0);
;         unsigned nloc = b.st[0], nx = b.st[1];
;         if (nloc == 0u) { xcd_barrier_complete(bar, b.x, nloc, nx); b.st[0] = nloc; b.st[1] = nx; }
;         const unsigned old = xb_add(&bar[XB_XSUB(b.x)], 1u);
;         const unsigned gen = old / nloc;
;         if (old + 1u == (gen + 1u) * nloc) {
;             __builtin_amdgcn_fence(__ATOMIC_RELEASE, "agent");
;             asm volatile("s_waitcnt vmcnt(0)" ::: "memory");
;             const unsigned og = xb_add(&bar[XB_TOP], 1u);
;             const unsigned tg = og / nx;
;             if (og + 1u == (tg + 1u) * nx) xb_add(&bar[XB_TOPGEN], 1u);
;             else XB_SPIN(xb_ld(&bar[XB_TOPGEN]) == tg, bar);
;             __builtin_amdgcn_fence(__ATOMIC_ACQUIRE, "agent");
;             xb_add(&bar[XB_XGEN(b.x)], 1u);
;             asm volatile("s_waitcnt vmcnt(0)" ::: "memory");
;         } else {
;             XB_SPIN(xb_ld(&bar[XB_XGEN(b.x)]) == gen, bar);
.LBB0_358:
	v_readlane_b32 s4, v251, 30
	v_readlane_b32 s5, v251, 31
	v_cvt_f32_u32_e32 v1, v3
	v_sub_u32_e32 v5, 0, v3
	v_rcp_iflag_f32_e32 v1, v1
	s_nop 1
	buffer_inv sc1
	global_atomic_add v4, v187, v224, s[4:5] sc0
	v_mul_f32_e32 v1, 0x4f7ffffe, v1
	v_cvt_u32_f32_e32 v1, v1
	v_mul_lo_u32 v5, v5, v1
	v_mul_hi_u32 v5, v1, v5
	v_add_u32_e32 v1, v1, v5
	s_waitcnt vmcnt(0)
	v_mul_hi_u32 v1, v4, v1
	v_mul_lo_u32 v5, v1, v3
	v_sub_u32_e32 v5, v4, v5
	v_add_u32_e32 v6, 1, v1
	v_cmp_ge_u32_e32 vcc, v5, v3
	v_add_u32_e32 v4, 1, v4
	s_nop 0
	v_cndmask_b32_e32 v1, v1, v6, vcc
	v_sub_u32_e32 v6, v5, v3
	v_cndmask_b32_e32 v5, v5, v6, vcc
	v_add_u32_e32 v6, 1, v1
	v_cmp_ge_u32_e32 vcc, v5, v3
	s_nop 1
	v_cndmask_b32_e32 v1, v1, v6, vcc
	v_mul_lo_u32 v5, v3, v1
	v_add_u32_e32 v3, v5, v3
	v_cmp_ne_u32_e32 vcc, v4, v3
	s_and_saveexec_b64 s[4:5], vcc
	s_xor_b64 s[4:5], exec, s[4:5]
	s_cbranch_execz .LBB0_372
	v_readlane_b32 s6, v251, 32
	v_readlane_b32 s7, v251, 33
	s_waitcnt lgkmcnt(0)
	s_nop 3
	global_load_dword v2, v187, s[6:7] sc1
	s_waitcnt vmcnt(0)
	v_cmp_eq_u32_e32 vcc, v2, v1
	s_and_saveexec_b64 s[6:7], vcc
	s_cbranch_execz .LBB0_371
	s_mov_b32 s20, 1
	s_mov_b64 s[8:9], 0
	s_branch .LBB0_362

; __device__ __forceinline__ unsigned xb_ld(unsigned* p)              { return __hip_atomic_load(p, __ATOMIC_RELAXED, __HIP_MEMORY_SCOPE_AGENT); }
; __device__ __forceinline__ unsigned xb_add(unsigned* p, unsigned v) { return __hip_atomic_fetch_add(p, v, __ATOMIC_RELAXED, __HIP_MEMORY_SCOPE_AGENT); }
; #define XB_SPIN(cond, bar) do { unsigned _sp = 0; while (cond) { __builtin_amdgcn_s_sleep(1); \
;     if ((++_sp & 255u) == 0u) { if (xb_ld(&(bar)[XB_TMO])) break; if (_sp > XB_SPIN_CAP) { atomicAdd(&(bar)[XB_TMO], 1u); break; } } } } while (0)
; __device__ __forceinline__ void xcd_barrier(const XcdBarrier& b) {
;     ...
;         __builtin_amdgcn_s_waitcnt(0);
;         unsigned nloc = b.st[0], nx = b.st[1];
;         if (nloc == 0u) { xcd_barrier_complete(bar, b.x, nloc, nx); b.st[0] = nloc; b.st[1] = nx; }
;         const unsigned old = xb_add(&bar[XB_XSUB(b.x)], 1u);
;         const unsigned gen = old / nloc;
;         if (old + 1u == (gen + 1u) * nloc) {
;             __builtin_amdgcn_fence(__ATOMIC_RELEASE, "agent");
;             asm volatile("s_waitcnt vmcnt(0)" ::: "memory");
;             const unsigned og = xb_add(&bar[XB_TOP], 1u);
;             const unsigned tg = og / nx;
;             if (og + 1u == (tg + 1u) * nx) xb_add(&bar[XB_TOPGEN], 1u);
;             else XB_SPIN(xb_ld(&bar[XB_TOPGEN]) == tg, bar);
;             __builtin_amdgcn_fence(__ATOMIC_ACQUIRE, "agent");
;             xb_add(&bar[XB_XGEN(b.x)], 1u);
;             asm volatile("s_waitcnt vmcnt(0)" ::: "memory");
;         } else {
;             XB_SPIN(xb_ld(&bar[XB_XGEN(b.x)]) == gen, bar);
.LBB0_798:
	v_readlane_b32 s6, v251, 30
	v_readlane_b32 s7, v251, 31
	v_cvt_f32_u32_e32 v1, v3
	v_sub_u32_e32 v5, 0, v3
	v_rcp_iflag_f32_e32 v1, v1
	s_nop 1
	buffer_inv sc1
	global_atomic_add v4, v187, v224, s[6:7] sc0
	v_mul_f32_e32 v1, 0x4f7ffffe, v1
	v_cvt_u32_f32_e32 v1, v1
	v_mul_lo_u32 v5, v5, v1
	v_mul_hi_u32 v5, v1, v5
	v_add_u32_e32 v1, v1, v5
	s_waitcnt vmcnt(0)
	v_mul_hi_u32 v1, v4, v1
	v_mul_lo_u32 v5, v1, v3
	v_sub_u32_e32 v5, v4, v5
	v_add_u32_e32 v6, 1, v1
	v_cmp_ge_u32_e32 vcc, v5, v3
	v_add_u32_e32 v4, 1, v4
	s_nop 0
	v_cndmask_b32_e32 v1, v1, v6, vcc
	v_sub_u32_e32 v6, v5, v3
	v_cndmask_b32_e32 v5, v5, v6, vcc
	v_add_u32_e32 v6, 1, v1
	v_cmp_ge_u32_e32 vcc, v5, v3
	s_nop 1
	v_cndmask_b32_e32 v1, v1, v6, vcc
	v_mul_lo_u32 v5, v3, v1
	v_add_u32_e32 v3, v5, v3
	v_cmp_ne_u32_e32 vcc, v4, v3
	s_and_saveexec_b64 s[6:7], vcc
	s_xor_b64 s[6:7], exec, s[6:7]
	s_cbranch_execz .LBB0_812
	v_readlane_b32 s8, v251, 32
	v_readlane_b32 s9, v251, 33
	s_waitcnt lgkmcnt(0)
	s_nop 3
	global_load_dword v2, v187, s[8:9] sc1
	s_waitcnt vmcnt(0)
	v_cmp_eq_u32_e32 vcc, v2, v1
	s_and_saveexec_b64 s[8:9], vcc
	s_cbranch_execz .LBB0_811
	s_mov_b32 s23, 1
	s_mov_b64 s[10:11], 0
	s_branch .LBB0_802

; __device__ __forceinline__ unsigned xb_ld(unsigned* p)              { return __hip_atomic_load(p, __ATOMIC_RELAXED, __HIP_MEMORY_SCOPE_AGENT); }
; #define XB_SPIN(cond, bar) do { unsigned _sp = 0; while (cond) { __builtin_amdgcn_s_sleep(1); \
;     if ((++_sp & 255u) == 0u) { if (xb_ld(&(bar)[XB_TMO])) break; if (_sp > XB_SPIN_CAP) { atomicAdd(&(bar)[XB_TMO], 1u); break; } } } } while (0)
; __device__ __forceinline__ void xcd_barrier(const XcdBarrier& b) {
;     ...
;             XB_SPIN(xb_ld(&bar[XB_XGEN(b.x)]) == gen, bar);
;             __builtin_amdgcn_fence(__ATOMIC_ACQUIRE, "agent");
;             asm volatile("s_waitcnt vmcnt(0)" ::: "memory");
.LBB0_811:
	s_or_b64 exec, exec, s[8:9]
	s_waitcnt vmcnt(0)
	s_waitcnt vmcnt(0)

; __device__ __forceinline__ unsigned xb_ld(unsigned* p)              { return __hip_atomic_load(p, __ATOMIC_RELAXED, __HIP_MEMORY_SCOPE_AGENT); }
; __device__ __forceinline__ unsigned xb_add(unsigned* p, unsigned v) { return __hip_atomic_fetch_add(p, v, __ATOMIC_RELAXED, __HIP_MEMORY_SCOPE_AGENT); }
; #define XB_SPIN(cond, bar) do { unsigned _sp = 0; while (cond) { __builtin_amdgcn_s_sleep(1); \
;     if ((++_sp & 255u) == 0u) { if (xb_ld(&(bar)[XB_TMO])) break; if (_sp > XB_SPIN_CAP) { atomicAdd(&(bar)[XB_TMO], 1u); break; } } } } while (0)
; __device__ __forceinline__ void xcd_barrier(const XcdBarrier& b) {
;     ...
;             const unsigned og = xb_add(&bar[XB_TOP], 1u);
;             const unsigned tg = og / nx;
;             if (og + 1u == (tg + 1u) * nx) xb_add(&bar[XB_TOPGEN], 1u);
;             else XB_SPIN(xb_ld(&bar[XB_TOPGEN]) == tg, bar);
;             __builtin_amdgcn_fence(__ATOMIC_ACQUIRE, "agent");
;             xb_add(&bar[XB_XGEN(b.x)], 1u);
;             asm volatile("s_waitcnt vmcnt(0)" ::: "memory");
.LBB0_829:
	s_or_b64 exec, exec, s[6:7]
	v_readlane_b32 s6, v251, 32
	v_readlane_b32 s7, v251, 33
	s_waitcnt vmcnt(0)
	s_nop 3
	global_atomic_add v187, v224, s[6:7]
	s_waitcnt vmcnt(0)
